# v8 plus DSA: no workgroup barrier between selection and attention (per-wave V staging moved into the wave's own score rows), SIMD partners desynchronise
# speedup vs baseline: 1.0041x; 1.0041x over previous
.LBB0_773:
	s_or_b64 exec, exec, s[6:7]
	s_lshl_b64 s[6:7], s[42:43], 19
	s_add_u32 s50, s66, s6
	s_addc_u32 s51, s67, s7
	s_lshl_b32 s6, s5, 2
	s_add_i32 s6, s6, 0
	s_add_i32 s6, s6, 0x22000
	v_mov_b32_e32 v0, s6
	s_waitcnt lgkmcnt(0)
	ds_read_b32 v0, v0
	s_lshl_b32 s7, s4, 10
	s_add_i32 s7, s7, 0
	v_lshrrev_b32_e32 v147, 2, v245
	v_and_b32_e32 v44, 3, v146
	s_add_i32 s7, s7, 0x20000
	s_waitcnt lgkmcnt(0)
	v_cmp_gt_i32_e32 vcc, 1, v0
	v_readlane_b32 s24, v255, 30
	v_readfirstlane_b32 s6, v0
	v_lshlrev_b32_e32 v246, 4, v44
	s_and_b64 vcc, exec, vcc
	v_lshl_add_u32 v45, v147, 1, s7
	v_readlane_b32 s25, v255, 31
	v_readlane_b32 s26, v255, 18
	s_cbranch_vccnz .LBB0_775
	ds_read_u16 v0, v45
	s_waitcnt lgkmcnt(0)
	v_lshl_or_b32 v4, v0, 8, v246
	global_load_dwordx4 v[0:3], v4, s[50:51]
	s_nop 0
	global_load_dwordx4 v[4:7], v4, s[50:51] offset:64

.LBB0_783:
	v_bfe_u32 v45, v245, 2, 2
	s_mul_i32 s6, s4, 0x4000
	v_lshl_or_b32 v45, v49, 2, v45
	s_or_b32 s7, s5, 1
	s_add_i32 s6, s6, 0
	v_mul_u32_u24_e32 v45, 0x90, v45
	v_lshlrev_b32_e32 v44, 3, v44
	s_lshl_b32 s8, s7, 2
	v_add3_u32 v249, v45, v44, s6
	v_lshlrev_b32_e32 v45, 4, v245
	s_add_i32 s12, s8, 0
	s_lshl_b32 s7, s7, 9
	v_readlane_b32 s8, v255, 44
	v_lshrrev_b32_e32 v247, 3, v245
	v_or_b32_e32 v46, v74, v49
	v_lshlrev_b32_e32 v44, 6, v245
	v_cmp_lt_u32_e64 s[38:39], 7, v71
	v_and_b32_e32 v250, 0x70, v45
	s_add_i32 s7, s7, 0
	v_mov_b32_e32 v45, s6
	s_movk_i32 s6, 0x90
	v_lshlrev_b32_e32 v70, 1, v71
	v_mov_b32_e32 v71, v48
	v_readlane_b32 s9, v255, 45
	v_lshlrev_b32_e32 v248, 2, v46
	v_and_b32_e32 v44, 0x1c0, v44
	v_lshlrev_b32_e32 v46, 3, v49
	s_add_i32 s7, s7, 0x20000
	v_mad_u32_u24 v45, v247, s6, v45
	v_lshl_add_u64 v[70:71], s[8:9], 0, v[70:71]
	v_lshlrev_b32_e32 v72, 9, v49
	v_mov_b32_e32 v73, v48
	s_add_i32 s12, s12, 0x22000
	v_cmp_gt_u32_e64 s[40:41], 32, v245
	v_lshl_add_u32 v251, v147, 1, s7
	v_lshl_add_u64 v[148:149], v[70:71], 0, v[72:73]
	s_mov_b32 s8, 0
	s_mov_b64 s[44:45], -1
	v_lshlrev_b32_e32 v150, 1, v44
	v_lshlrev_b32_e32 v152, 1, v46
	v_add_u32_e32 v252, v45, v250
	s_branch .LBB0_785
